# baseline (speedup 1.0000x reference)
_Z13attn11_kernelILi4EEvPc:
	s_ashr_i32 s5, s2, 3
	s_load_dwordx2 s[12:13], s[0:1], 0x0
	s_lshr_b32 s4, s5, 29
	s_lshl_b32 s3, s2, 4
	s_add_i32 s6, s5, s4
	s_and_b32 s3, s3, 0x70
	s_ashr_i32 s4, s6, 3
	s_add_i32 s4, s3, s4
	s_and_b32 s3, s6, 0x1fffff8
	s_sub_i32 s3, s5, s3
	v_lshrrev_b32_e32 v1, 6, v0
	s_waitcnt lgkmcnt(0)
	s_add_u32 s14, s12, 0x2500000
	v_lshlrev_b32_e32 v192, 5, v1
	s_addc_u32 s15, s13, 0
	s_ashr_i32 s5, s4, 31
	s_mul_i32 s6, s4, 0x12000
	v_lshl_or_b32 v172, s3, 7, v192
	s_mul_hi_i32 s3, s4, 0x12000
	s_add_u32 s8, s14, s6
	s_addc_u32 s9, s15, s3
	s_add_u32 s16, s12, 0x3700000
	v_lshlrev_b32_e32 v169, 4, v0
	s_addc_u32 s17, s13, 0
	s_add_u32 s10, s16, s6
	v_add_u32_e32 v193, 0, v169
	v_lshrrev_b32_e32 v2, 2, v0
	v_bitop3_b32 v3, v169, 48, v0 bitop3:0x48
	s_addc_u32 s11, s17, s3
	s_mov_b64 s[46:47], s[8:9]
	s_mov_b64 s[48:49], s[10:11]
	s_mov_b64 s[50:51], s[14:15]
	s_mov_b64 s[52:53], s[16:17]
	v_readfirstlane_b32 s3, v193
	v_add_u32_e32 v4, 0x8000, v193
	v_lshl_or_b32 v170, v2, 6, v3
	v_mul_u32_u24_e32 v2, 0x480, v2
	v_mov_b32_e32 v171, 0
	s_mov_b32 m0, s3
	v_readfirstlane_b32 s3, v4
	v_add_u32_e32 v6, 0x2000, v193
	v_or_b32_e32 v2, v2, v3
	v_lshl_add_u64 v[174:175], s[8:9], 0, v[170:171]
	v_mov_b32_e32 v3, v171
	global_load_lds_dwordx4 v170, s[8:9]
	v_mov_b32_e32 v220, v170
	s_mov_b32 m0, s3
	s_mov_b64 s[8:9], 0x1000
	v_readfirstlane_b32 s6, v6
	v_add_u32_e32 v6, 0x4000, v193
	v_lshl_add_u64 v[176:177], s[10:11], 0, v[2:3]
	global_load_lds_dwordx4 v2, s[10:11]
	v_mov_b32_e32 v221, v2
	v_lshl_add_u64 v[4:5], v[174:175], 0, s[8:9]
	s_mov_b32 m0, s6
	s_mov_b64 s[10:11], 0x2000
	v_readfirstlane_b32 s6, v6
	v_add_u32_e32 v6, 0xa000, v193
	global_load_lds_dwordx4 v[4:5], off
	v_lshl_add_u64 v[4:5], v[174:175], 0, s[10:11]
	s_mov_b32 m0, s6
	v_readfirstlane_b32 s6, v6
	s_add_u32 s18, s12, 0x1500000
	global_load_lds_dwordx4 v[4:5], off
	v_lshl_add_u64 v[4:5], v[176:177], 0, 64
	s_mov_b32 m0, s6
	s_addc_u32 s19, s13, 0
	s_lshl_b64 s[20:21], s[4:5], 10
	v_ashrrev_i32_e32 v173, 31, v172
	v_and_b32_e32 v168, 31, v0
	global_load_lds_dwordx4 v[4:5], off
	v_lshl_add_u64 v[4:5], s[20:21], 0, v[172:173]
	v_or_b32_e32 v4, v4, v168
	v_lshlrev_b64 v[4:5], 6, v[4:5]
	v_lshl_add_u64 v[4:5], s[18:19], 0, v[4:5]
	v_and_b32_e32 v6, 32, v0
	v_mov_b32_e32 v7, v171
	v_lshl_add_u64 v[4:5], v[4:5], 0, v[6:7]
	global_load_dwordx4 v[152:155], v[4:5], off
	global_load_dwordx4 v[156:159], v[4:5], off offset:16
	v_and_b32_e32 v4, 60, v0
	v_lshlrev_b32_e32 v5, 2, v0
	s_add_u32 s0, s0, 8
	s_movk_i32 s5, 0xa00
	v_lshlrev_b32_e32 v184, 7, v4
	v_or_b32_e32 v4, 64, v4
	v_bitop3_b32 v195, v5, v6, 48 bitop3:0x6c
	v_lshl_add_u64 v[178:179], s[14:15], 0, v[170:171]
	v_lshl_add_u64 v[180:181], s[16:17], 0, v[2:3]
	s_addc_u32 s1, s1, 0
	v_mad_u32_u24 v1, v1, s5, 0
	v_lshrrev_b32_e32 v2, 3, v0
	s_movk_i32 s5, 0x50
	v_and_b32_e32 v170, 48, v169
	v_bfe_u32 v0, v0, 2, 4
	v_lshrrev_b32_e32 v5, 2, v4
	v_mov_b32_e32 v144, 0x38383838
	v_bfe_u32 v226, v169, 6, 1
	v_bfe_u32 v227, v169, 8, 1
	v_cmp_eq_u32_e32 vcc, v226, v227
	s_nop 1
	v_cndmask_b32_e32 v144, 0, v144, vcc
	v_lshl_add_u64 v[182:183], s[18:19], 0, v[6:7]
	v_and_b32_e32 v2, 4, v2
	v_mad_u32_u24 v3, v168, s5, v1
	s_add_u32 s12, s12, 0x4900000
	v_add_u32_e32 v1, v1, v170
	v_mul_u32_u24_e32 v0, 0x50, v0
	v_mul_u32_u24_e32 v5, 0x50, v5
	s_movk_i32 s18, 0xffc0
	v_lshlrev_b32_e32 v199, 6, v168
	s_mov_b32 s7, 0
	s_movk_i32 s3, 0x2000
	s_movk_i32 s33, 0x4000
	v_mov_b32_e32 v173, 0x74747474
	v_mov_b32_e32 v194, 0x7f7f7f7f
	v_mov_b32_e32 v145, v144
	v_mov_b32_e32 v146, v144
	v_mov_b32_e32 v147, v144
	v_mov_b32_e32 v148, v144
	v_mov_b32_e32 v149, v144
	v_mov_b32_e32 v150, v144
	v_mov_b32_e32 v151, v144
	s_addc_u32 s13, s13, 0
	v_mov_b32_e32 v185, v171
	v_lshlrev_b32_e32 v186, 7, v4
	v_mov_b32_e32 v187, v171
	s_mov_b64 s[30:31], -1
	s_mov_b64 s[14:15], 0x3000
	s_mov_b64 s[16:17], 0xc0
	s_mov_b32 s19, -1
	s_mov_b32 s5, 0xff61b1e6
	s_mov_b32 s36, 0x41000000
	s_mov_b64 s[20:21], 0x80
	s_mov_b64 s[22:23], 0x11000
	s_mov_b64 s[24:25], 0x400
	s_mov_b64 s[26:27], 0x440
	s_mov_b32 s37, 0x42800000
	v_add_u32_e32 v196, v3, v2
	v_add_u32_e32 v197, v1, v0
	v_add_u32_e32 v198, v1, v5
	v_add_u32_e32 v197, 0x10000, v197
	v_add_u32_e32 v198, 0x10000, v198
	v_mov_b32_e32 v0, v171
	v_mov_b32_e32 v1, v171
	v_mov_b32_e32 v2, v171
	v_mov_b32_e32 v3, v171
	v_mov_b32_e32 v4, v171
	v_mov_b32_e32 v5, v171
	v_mov_b32_e32 v6, v171
	v_mov_b32_e32 v8, v171
	v_mov_b32_e32 v9, v171
	v_mov_b32_e32 v10, v171
	v_mov_b32_e32 v11, v171
	v_mov_b32_e32 v12, v171
	v_mov_b32_e32 v13, v171
	v_mov_b32_e32 v14, v171
	v_mov_b32_e32 v15, v171
	s_mov_b32 s38, 0
	v_mov_b32_e32 v160, v171
	v_mov_b32_e32 v161, v171
	v_mov_b32_e32 v162, v171
	v_mov_b32_e32 v163, v171
	v_mov_b32_e32 v164, v171
	v_mov_b32_e32 v165, v171
	v_mov_b32_e32 v166, v171
	v_mov_b32_e32 v167, v171
	v_xor_b32_e32 v200, 16, v195
	v_add_u32_e32 v201, 0, v199
	v_add_u32_e32 v222, v199, v195
	v_add_u32_e32 v223, v199, v200
	v_readfirstlane_b32 s40, v169
	v_add_u32_e32 v224, 0x8000, v222
	v_add_u32_e32 v225, 0x8000, v223
	v_add_u32_e32 v228, 0x1000, v220
	v_add_u32_e32 v229, 64, v221
	s_add_u32 s60, s40, 0x0
	s_add_u32 s61, s40, 0x2000
	s_add_u32 s62, s40, 0x4000
	s_add_u32 s63, s40, 0x6000
	s_add_u32 s64, s40, 0x8000
	s_add_u32 s65, s40, 0xa000
	s_add_u32 s66, s40, 0xc000
	s_add_u32 s67, s40, 0xe000
	v_mov_b32_e32 v202, 0x12000
	s_branch .LBB3_3

.LBB3_3:
	s_add_u32 s42, s46, 0x3000
	s_addc_u32 s43, s47, 0
	s_add_u32 s44, s48, 0x0
	s_addc_u32 s45, s49, 0
	v_mov_b64_e32 v[30:31], v[14:15]
	v_mov_b64_e32 v[28:29], v[12:13]
	v_mov_b64_e32 v[26:27], v[10:11]
	v_mov_b64_e32 v[24:25], v[8:9]
	v_mov_b64_e32 v[22:23], v[6:7]
	v_mov_b64_e32 v[20:21], v[4:5]
	v_mov_b64_e32 v[18:19], v[2:3]
	v_mov_b64_e32 v[16:17], v[0:1]
	v_add_u32_e32 v32, s38, v201
	s_waitcnt vmcnt(0) lgkmcnt(0)
	s_barrier
	v_add_u32_e32 v41, v32, v200
	v_add_u32_e32 v40, v32, v195
	ds_read_b128 v[36:39], v41
	ds_read_b128 v[32:35], v40
	ds_read_b128 v[48:51], v40 offset:2048
	ds_read_b128 v[52:55], v41 offset:2048
	s_waitcnt vmcnt(0) lgkmcnt(0)
	v_mfma_scale_f32_32x32x64_f8f6f4 v[32:47], v[32:39], v[152:159], v[16:31], v173, v194 op_sel_hi:[0,0,0]
	s_waitcnt vmcnt(2) lgkmcnt(0)
	s_barrier
	s_xor_b64 s[28:29], s[30:31], -1
	s_mov_b32 s6, -1
	s_nop 15
	v_max_f32_e32 v56, v33, v33
	v_mfma_scale_f32_32x32x64_f8f6f4 v[16:31], v[48:55], v[152:159], v[16:31], v173, v194 op_sel_hi:[0,0,0]
	v_max_f32_e32 v57, v32, v32
	v_max_f32_e32 v56, v57, v56
	s_nop 15
	s_nop 1
	v_max3_f32 v48, v34, v35, v17
	v_max3_f32 v49, v56, v16, v18
	v_max3_f32 v49, v49, v19, v36
	v_max3_f32 v48, v48, v38, v39
	v_max3_f32 v48, v48, v22, v23
	v_max3_f32 v49, v49, v37, v20
	v_max3_f32 v48, v48, v42, v43
	v_max3_f32 v49, v49, v21, v40
	v_max3_f32 v48, v48, v26, v27
	v_max3_f32 v49, v49, v41, v24
	v_max3_f32 v48, v48, v46, v47
	v_max3_f32 v49, v49, v25, v44
	v_max3_f32 v48, v48, v30, v31
	v_max3_f32 v49, v49, v45, v28
	v_max3_f32 v48, v49, v29, v48
	v_mov_b32_e32 v49, v48
	s_nop 1
	v_permlane32_swap_b32_e32 v48, v49
	v_max_f32_e32 v49, v49, v49
	v_max_f32_e32 v48, v48, v48
	v_max_f32_e32 v48, v48, v49
	v_sub_f32_e32 v95, v47, v48
	v_sub_f32_e32 v94, v46, v48
	v_sub_f32_e32 v93, v45, v48
	v_sub_f32_e32 v92, v44, v48
	v_sub_f32_e32 v91, v43, v48
	v_sub_f32_e32 v90, v42, v48
	v_sub_f32_e32 v89, v41, v48
	v_sub_f32_e32 v88, v40, v48
	v_sub_f32_e32 v87, v39, v48
	v_sub_f32_e32 v86, v38, v48
	v_sub_f32_e32 v85, v37, v48
	v_sub_f32_e32 v84, v36, v48
	v_sub_f32_e32 v83, v35, v48
	v_sub_f32_e32 v82, v34, v48
	v_sub_f32_e32 v81, v33, v48
	v_sub_f32_e32 v80, v32, v48
	v_sub_f32_e32 v111, v31, v48
	v_sub_f32_e32 v110, v30, v48
	v_sub_f32_e32 v109, v29, v48
	v_sub_f32_e32 v108, v28, v48
	v_sub_f32_e32 v107, v27, v48
	v_sub_f32_e32 v106, v26, v48
	v_sub_f32_e32 v105, v25, v48
	v_sub_f32_e32 v104, v24, v48
	v_sub_f32_e32 v103, v23, v48
	v_sub_f32_e32 v102, v22, v48
	v_sub_f32_e32 v101, v21, v48
	v_sub_f32_e32 v100, v20, v48
	v_sub_f32_e32 v99, v19, v48
	v_sub_f32_e32 v98, v18, v48
	v_sub_f32_e32 v97, v17, v48
	v_sub_f32_e32 v96, v16, v48
	v_xor_b32_e32 v64, 0x80000000, v48
	v_mov_b64_e32 v[46:47], v[14:15]
	v_mov_b64_e32 v[30:31], v[14:15]
	v_mov_b64_e32 v[62:63], v[14:15]
	v_mov_b32_e32 v65, v64
	v_mov_b32_e32 v66, v64
	v_mov_b32_e32 v67, v64
	v_mov_b32_e32 v68, v64
	v_mov_b32_e32 v69, v64
	v_mov_b32_e32 v70, v64
	v_mov_b32_e32 v71, v64
	v_mov_b32_e32 v72, v64
	v_mov_b32_e32 v73, v64
	v_mov_b32_e32 v74, v64
	v_mov_b32_e32 v75, v64
	v_mov_b32_e32 v76, v64
	v_mov_b32_e32 v77, v64
	v_mov_b32_e32 v78, v64
	v_mov_b32_e32 v79, v64
	v_mov_b64_e32 v[44:45], v[12:13]
	v_mov_b64_e32 v[42:43], v[10:11]
	v_mov_b64_e32 v[40:41], v[8:9]
	v_mov_b64_e32 v[38:39], v[6:7]
	v_mov_b64_e32 v[36:37], v[4:5]
	v_mov_b64_e32 v[34:35], v[2:3]
	v_mov_b64_e32 v[32:33], v[0:1]
	v_mov_b64_e32 v[28:29], v[12:13]
	v_mov_b64_e32 v[26:27], v[10:11]
	v_mov_b64_e32 v[24:25], v[8:9]
	v_mov_b64_e32 v[22:23], v[6:7]
	v_mov_b64_e32 v[20:21], v[4:5]
	v_mov_b64_e32 v[18:19], v[2:3]
	v_mov_b64_e32 v[16:17], v[0:1]
	v_mov_b64_e32 v[60:61], v[12:13]
	v_mov_b64_e32 v[58:59], v[10:11]
	v_mov_b64_e32 v[56:57], v[8:9]
	v_mov_b64_e32 v[54:55], v[6:7]
	v_mov_b64_e32 v[52:53], v[4:5]
	v_mov_b64_e32 v[50:51], v[2:3]
	v_mov_b64_e32 v[48:49], v[0:1]
	s_mov_b32 s39, 0
.Lat_loop:
	ds_read_b128 v[112:115], v222 offset:8192
	ds_read_b128 v[128:131], v222 offset:10240
	ds_read_b128 v[116:119], v223 offset:8192
	ds_read_b128 v[132:135], v223 offset:10240
	s_mov_b32 m0, s63
	s_add_u32 s44, s44, 128
	s_addc_u32 s45, s45, 0
	global_load_lds_dwordx4 v220, s[42:43]
	s_mov_b32 m0, s60
	s_nop 0
	global_load_lds_dwordx4 v228, s[42:43]
	s_setprio 1
	v_exp_f32_e32 v80, v80
	v_exp_f32_e32 v81, v81
	v_exp_f32_e32 v82, v82
	v_exp_f32_e32 v83, v83
	v_exp_f32_e32 v84, v84
	v_exp_f32_e32 v85, v85
	v_exp_f32_e32 v86, v86
	v_exp_f32_e32 v87, v87
	v_cvt_pk_fp8_f32 v160, v80, v81
	v_cvt_pk_fp8_f32 v161, v84, v85
	v_exp_f32_e32 v88, v88
	v_exp_f32_e32 v89, v89
	v_cvt_pk_fp8_f32 v160, v82, v83 op_sel:[0,0,1]
	v_cvt_pk_fp8_f32 v161, v86, v87 op_sel:[0,0,1]
	v_exp_f32_e32 v90, v90
	v_exp_f32_e32 v91, v91
	v_exp_f32_e32 v92, v92
	v_exp_f32_e32 v93, v93
	v_exp_f32_e32 v94, v94
	v_exp_f32_e32 v95, v95
	s_waitcnt lgkmcnt(0)
	v_mfma_scale_f32_32x32x64_f8f6f4 v[112:127], v[112:119], v[152:159], v[64:79], v173, v194 op_sel_hi:[0,0,0]
	s_setprio 0
	ds_read_b128 v[80:83], v224 offset:0
	ds_read_b128 v[212:215], v224 offset:2048
	ds_read_b128 v[84:87], v225 offset:0
	ds_read_b128 v[216:219], v225 offset:2048
	v_cvt_pk_fp8_f32 v162, v88, v89
	v_cvt_pk_fp8_f32 v163, v92, v93
	v_exp_f32_e32 v96, v96
	v_exp_f32_e32 v97, v97
	v_cvt_pk_fp8_f32 v162, v90, v91 op_sel:[0,0,1]
	v_cvt_pk_fp8_f32 v163, v94, v95 op_sel:[0,0,1]
	v_exp_f32_e32 v98, v98
	v_exp_f32_e32 v99, v99
	v_exp_f32_e32 v100, v100
	v_exp_f32_e32 v101, v101
	v_exp_f32_e32 v102, v102
	v_exp_f32_e32 v103, v103
	v_mfma_scale_f32_32x32x64_f8f6f4 v[128:143], v[128:135], v[152:159], v[64:79], v173, v194 op_sel_hi:[0,0,0]
	v_cvt_pk_fp8_f32 v164, v96, v97
	v_cvt_pk_fp8_f32 v165, v100, v101
	v_exp_f32_e32 v104, v104
	v_exp_f32_e32 v105, v105
	v_cvt_pk_fp8_f32 v164, v98, v99 op_sel:[0,0,1]
	v_cvt_pk_fp8_f32 v165, v102, v103 op_sel:[0,0,1]
	v_exp_f32_e32 v106, v106
	v_exp_f32_e32 v107, v107
	v_exp_f32_e32 v108, v108
	v_exp_f32_e32 v109, v109
	v_exp_f32_e32 v110, v110
	v_exp_f32_e32 v111, v111
	s_nop 0
	v_cvt_pk_fp8_f32 v166, v104, v105
	v_cvt_pk_fp8_f32 v167, v108, v109
	v_cvt_pk_fp8_f32 v166, v106, v107 op_sel:[0,0,1]
	v_cvt_pk_fp8_f32 v167, v110, v111 op_sel:[0,0,1]
	s_setprio 2
	s_waitcnt lgkmcnt(0)
	v_mfma_scale_f32_32x32x64_f8f6f4 v[32:47], v[80:87], v[160:167], v[32:47], v194, v194 op_sel_hi:[0,0,0]
	ds_read_b128 v[80:83], v222 offset:16384
	ds_read_b128 v[96:99], v222 offset:18432
	ds_read_b128 v[84:87], v223 offset:16384
	ds_read_b128 v[100:103], v223 offset:18432
	v_max3_f32 v227, v112, s5, v113
	v_max3_f32 v227, v227, v114, v115
	v_max3_f32 v227, v227, v116, v117
	v_max3_f32 v227, v227, v118, v119
	v_max3_f32 v227, v227, v120, v121
	v_max3_f32 v227, v227, v122, v123
	v_max3_f32 v227, v227, v124, v125
	v_max3_f32 v227, v227, v126, v127
	s_mov_b32 m0, s66
	s_add_u32 s42, s42, 0x2000
	s_addc_u32 s43, s43, 0
	global_load_lds_dwordx4 v221, s[44:45]
	v_mfma_scale_f32_32x32x64_f8f6f4 v[16:31], v[212:219], v[160:167], v[16:31], v194, v194 op_sel_hi:[0,0,0]
	v_max3_f32 v226, v128, s5, v129
	v_max3_f32 v226, v226, v130, v131
	v_max3_f32 v226, v226, v132, v133
	v_max3_f32 v226, v226, v134, v135
	v_max3_f32 v226, v226, v136, v137
	v_max3_f32 v226, v226, v138, v139
	v_max3_f32 v226, v226, v140, v141
	v_max3_f32 v226, v226, v142, v143
	s_mov_b32 m0, s67
	s_nop 0
	global_load_lds_dwordx4 v229, s[44:45]
	v_mfma_scale_f32_16x16x128_f8f6f4 v[48:51], v[144:151], v[160:167], v[48:51], v194, v194 op_sel_hi:[0,0,0]
	s_setprio 0
	v_max_f32_e32 v226, v227, v226
	v_cmp_lt_f32_e32 vcc, s36, v226
	s_cbranch_vccnz .Lat_rare_L1

.Lat_back_L2:
	s_waitcnt vmcnt(0) lgkmcnt(0)
	s_barrier
	ds_read_b128 v[112:115], v222 offset:24576
	ds_read_b128 v[128:131], v222 offset:26624
	ds_read_b128 v[116:119], v223 offset:24576
	ds_read_b128 v[132:135], v223 offset:26624
	s_mov_b32 m0, s61
	s_add_u32 s44, s44, 128
	s_addc_u32 s45, s45, 0
	global_load_lds_dwordx4 v220, s[42:43]
	s_mov_b32 m0, s62
	s_nop 0
	global_load_lds_dwordx4 v228, s[42:43]
	s_setprio 1
	v_exp_f32_e32 v80, v80
	v_exp_f32_e32 v81, v81
	v_exp_f32_e32 v82, v82
	v_exp_f32_e32 v83, v83
	v_exp_f32_e32 v84, v84
	v_exp_f32_e32 v85, v85
	v_exp_f32_e32 v86, v86
	v_exp_f32_e32 v87, v87
	v_cvt_pk_fp8_f32 v160, v80, v81
	v_cvt_pk_fp8_f32 v161, v84, v85
	v_exp_f32_e32 v88, v88
	v_exp_f32_e32 v89, v89
	v_cvt_pk_fp8_f32 v160, v82, v83 op_sel:[0,0,1]
	v_cvt_pk_fp8_f32 v161, v86, v87 op_sel:[0,0,1]
	v_exp_f32_e32 v90, v90
	v_exp_f32_e32 v91, v91
	v_exp_f32_e32 v92, v92
	v_exp_f32_e32 v93, v93
	v_exp_f32_e32 v94, v94
	v_exp_f32_e32 v95, v95
	s_waitcnt lgkmcnt(0)
	v_mfma_scale_f32_32x32x64_f8f6f4 v[112:127], v[112:119], v[152:159], v[64:79], v173, v194 op_sel_hi:[0,0,0]
	s_setprio 0
	ds_read_b128 v[80:83], v224 offset:16384
	ds_read_b128 v[212:215], v224 offset:18432
	ds_read_b128 v[84:87], v225 offset:16384
	ds_read_b128 v[216:219], v225 offset:18432
	v_cvt_pk_fp8_f32 v162, v88, v89
	v_cvt_pk_fp8_f32 v163, v92, v93
	v_exp_f32_e32 v96, v96
	v_exp_f32_e32 v97, v97
	v_cvt_pk_fp8_f32 v162, v90, v91 op_sel:[0,0,1]
	v_cvt_pk_fp8_f32 v163, v94, v95 op_sel:[0,0,1]
	v_exp_f32_e32 v98, v98
	v_exp_f32_e32 v99, v99
	v_exp_f32_e32 v100, v100
	v_exp_f32_e32 v101, v101
	v_exp_f32_e32 v102, v102
	v_exp_f32_e32 v103, v103
	v_mfma_scale_f32_32x32x64_f8f6f4 v[128:143], v[128:135], v[152:159], v[64:79], v173, v194 op_sel_hi:[0,0,0]
	v_cvt_pk_fp8_f32 v164, v96, v97
	v_cvt_pk_fp8_f32 v165, v100, v101
	v_exp_f32_e32 v104, v104
	v_exp_f32_e32 v105, v105
	v_cvt_pk_fp8_f32 v164, v98, v99 op_sel:[0,0,1]
	v_cvt_pk_fp8_f32 v165, v102, v103 op_sel:[0,0,1]
	v_exp_f32_e32 v106, v106
	v_exp_f32_e32 v107, v107
	v_exp_f32_e32 v108, v108
	v_exp_f32_e32 v109, v109
	v_exp_f32_e32 v110, v110
	v_exp_f32_e32 v111, v111
	s_nop 0
	v_cvt_pk_fp8_f32 v166, v104, v105
	v_cvt_pk_fp8_f32 v167, v108, v109
	v_cvt_pk_fp8_f32 v166, v106, v107 op_sel:[0,0,1]
	v_cvt_pk_fp8_f32 v167, v110, v111 op_sel:[0,0,1]
	s_setprio 2
	s_waitcnt lgkmcnt(0)
	v_mfma_scale_f32_32x32x64_f8f6f4 v[32:47], v[80:87], v[160:167], v[32:47], v194, v194 op_sel_hi:[0,0,0]
	ds_read_b128 v[80:83], v222 offset:0
	ds_read_b128 v[96:99], v222 offset:2048
	ds_read_b128 v[84:87], v223 offset:0
	ds_read_b128 v[100:103], v223 offset:2048
	v_max3_f32 v227, v112, s5, v113
	v_max3_f32 v227, v227, v114, v115
	v_max3_f32 v227, v227, v116, v117
	v_max3_f32 v227, v227, v118, v119
	v_max3_f32 v227, v227, v120, v121
	v_max3_f32 v227, v227, v122, v123
	v_max3_f32 v227, v227, v124, v125
	v_max3_f32 v227, v227, v126, v127
	s_mov_b32 m0, s64
	s_add_u32 s42, s42, 0x2000
	s_addc_u32 s43, s43, 0
	global_load_lds_dwordx4 v221, s[44:45]
	v_mfma_scale_f32_32x32x64_f8f6f4 v[16:31], v[212:219], v[160:167], v[16:31], v194, v194 op_sel_hi:[0,0,0]
	v_max3_f32 v226, v128, s5, v129
	v_max3_f32 v226, v226, v130, v131
	v_max3_f32 v226, v226, v132, v133
	v_max3_f32 v226, v226, v134, v135
	v_max3_f32 v226, v226, v136, v137
	v_max3_f32 v226, v226, v138, v139
	v_max3_f32 v226, v226, v140, v141
	v_max3_f32 v226, v226, v142, v143
	s_mov_b32 m0, s65
	s_nop 0
	global_load_lds_dwordx4 v229, s[44:45]
	v_mfma_scale_f32_16x16x128_f8f6f4 v[48:51], v[144:151], v[160:167], v[48:51], v194, v194 op_sel_hi:[0,0,0]
	s_setprio 0
	v_max_f32_e32 v226, v227, v226
	v_cmp_lt_f32_e32 vcc, s36, v226
	s_cbranch_vccnz .Lat_rare_L3

.Lat_back_L4:
	s_waitcnt vmcnt(0) lgkmcnt(0)
	s_barrier
	s_add_u32 s39, s39, 1
	s_cmp_lt_u32 s39, 3
	s_cbranch_scc1 .Lat_loop
	ds_read_b128 v[112:115], v222 offset:8192
	ds_read_b128 v[128:131], v222 offset:10240
	ds_read_b128 v[116:119], v223 offset:8192
	ds_read_b128 v[132:135], v223 offset:10240
	s_mov_b32 m0, s63
	s_add_u32 s44, s44, 128
	s_addc_u32 s45, s45, 0
	global_load_lds_dwordx4 v220, s[42:43]
	s_mov_b32 m0, s60
	s_nop 0
	global_load_lds_dwordx4 v228, s[42:43]
	s_setprio 1
	v_exp_f32_e32 v80, v80
	v_exp_f32_e32 v81, v81
	v_exp_f32_e32 v82, v82
	v_exp_f32_e32 v83, v83
	v_exp_f32_e32 v84, v84
	v_exp_f32_e32 v85, v85
	v_exp_f32_e32 v86, v86
	v_exp_f32_e32 v87, v87
	v_cvt_pk_fp8_f32 v160, v80, v81
	v_cvt_pk_fp8_f32 v161, v84, v85
	v_exp_f32_e32 v88, v88
	v_exp_f32_e32 v89, v89
	v_cvt_pk_fp8_f32 v160, v82, v83 op_sel:[0,0,1]
	v_cvt_pk_fp8_f32 v161, v86, v87 op_sel:[0,0,1]
	v_exp_f32_e32 v90, v90
	v_exp_f32_e32 v91, v91
	v_exp_f32_e32 v92, v92
	v_exp_f32_e32 v93, v93
	v_exp_f32_e32 v94, v94
	v_exp_f32_e32 v95, v95
	s_waitcnt lgkmcnt(0)
	v_mfma_scale_f32_32x32x64_f8f6f4 v[112:127], v[112:119], v[152:159], v[64:79], v173, v194 op_sel_hi:[0,0,0]
	s_setprio 0
	ds_read_b128 v[80:83], v224 offset:0
	ds_read_b128 v[212:215], v224 offset:2048
	ds_read_b128 v[84:87], v225 offset:0
	ds_read_b128 v[216:219], v225 offset:2048
	v_cvt_pk_fp8_f32 v162, v88, v89
	v_cvt_pk_fp8_f32 v163, v92, v93
	v_exp_f32_e32 v96, v96
	v_exp_f32_e32 v97, v97
	v_cvt_pk_fp8_f32 v162, v90, v91 op_sel:[0,0,1]
	v_cvt_pk_fp8_f32 v163, v94, v95 op_sel:[0,0,1]
	v_exp_f32_e32 v98, v98
	v_exp_f32_e32 v99, v99
	v_exp_f32_e32 v100, v100
	v_exp_f32_e32 v101, v101
	v_exp_f32_e32 v102, v102
	v_exp_f32_e32 v103, v103
	v_mfma_scale_f32_32x32x64_f8f6f4 v[128:143], v[128:135], v[152:159], v[64:79], v173, v194 op_sel_hi:[0,0,0]
	v_cvt_pk_fp8_f32 v164, v96, v97
	v_cvt_pk_fp8_f32 v165, v100, v101
	v_exp_f32_e32 v104, v104
	v_exp_f32_e32 v105, v105
	v_cvt_pk_fp8_f32 v164, v98, v99 op_sel:[0,0,1]
	v_cvt_pk_fp8_f32 v165, v102, v103 op_sel:[0,0,1]
	v_exp_f32_e32 v106, v106
	v_exp_f32_e32 v107, v107
	v_exp_f32_e32 v108, v108
	v_exp_f32_e32 v109, v109
	v_exp_f32_e32 v110, v110
	v_exp_f32_e32 v111, v111
	s_nop 0
	v_cvt_pk_fp8_f32 v166, v104, v105
	v_cvt_pk_fp8_f32 v167, v108, v109
	v_cvt_pk_fp8_f32 v166, v106, v107 op_sel:[0,0,1]
	v_cvt_pk_fp8_f32 v167, v110, v111 op_sel:[0,0,1]
	s_setprio 2
	s_waitcnt lgkmcnt(0)
	v_mfma_scale_f32_32x32x64_f8f6f4 v[32:47], v[80:87], v[160:167], v[32:47], v194, v194 op_sel_hi:[0,0,0]
	ds_read_b128 v[80:83], v222 offset:16384
	ds_read_b128 v[96:99], v222 offset:18432
	ds_read_b128 v[84:87], v223 offset:16384
	ds_read_b128 v[100:103], v223 offset:18432
	v_max3_f32 v227, v112, s5, v113
	v_max3_f32 v227, v227, v114, v115
	v_max3_f32 v227, v227, v116, v117
	v_max3_f32 v227, v227, v118, v119
	v_max3_f32 v227, v227, v120, v121
	v_max3_f32 v227, v227, v122, v123
	v_max3_f32 v227, v227, v124, v125
	v_max3_f32 v227, v227, v126, v127
	s_mov_b32 m0, s66
	s_add_u32 s42, s42, 0x2000
	s_addc_u32 s43, s43, 0
	global_load_lds_dwordx4 v221, s[44:45]
	v_mfma_scale_f32_32x32x64_f8f6f4 v[16:31], v[212:219], v[160:167], v[16:31], v194, v194 op_sel_hi:[0,0,0]
	v_max3_f32 v226, v128, s5, v129
	v_max3_f32 v226, v226, v130, v131
	v_max3_f32 v226, v226, v132, v133
	v_max3_f32 v226, v226, v134, v135
	v_max3_f32 v226, v226, v136, v137
	v_max3_f32 v226, v226, v138, v139
	v_max3_f32 v226, v226, v140, v141
	v_max3_f32 v226, v226, v142, v143
	s_mov_b32 m0, s67
	s_nop 0
	global_load_lds_dwordx4 v229, s[44:45]
	v_mfma_scale_f32_16x16x128_f8f6f4 v[48:51], v[144:151], v[160:167], v[48:51], v194, v194 op_sel_hi:[0,0,0]
	s_setprio 0
	v_max_f32_e32 v226, v227, v226
	v_cmp_lt_f32_e32 vcc, s36, v226
	s_cbranch_vccnz .Lat_rare_P13

.Lat_back_P14:
	s_waitcnt vmcnt(0) lgkmcnt(0)
	s_barrier
	ds_read_b128 v[112:115], v222 offset:24576
	ds_read_b128 v[128:131], v222 offset:26624
	ds_read_b128 v[116:119], v223 offset:24576
	ds_read_b128 v[132:135], v223 offset:26624
	s_mov_b32 m0, s61
	s_add_u32 s44, s44, 128
	s_addc_u32 s45, s45, 0
	global_load_lds_dwordx4 v220, s[42:43]
	s_setprio 1
	v_exp_f32_e32 v80, v80
	v_exp_f32_e32 v81, v81
	v_exp_f32_e32 v82, v82
	v_exp_f32_e32 v83, v83
	v_exp_f32_e32 v84, v84
	v_exp_f32_e32 v85, v85
	v_exp_f32_e32 v86, v86
	v_exp_f32_e32 v87, v87
	v_cvt_pk_fp8_f32 v160, v80, v81
	v_cvt_pk_fp8_f32 v161, v84, v85
	v_exp_f32_e32 v88, v88
	v_exp_f32_e32 v89, v89
	v_cvt_pk_fp8_f32 v160, v82, v83 op_sel:[0,0,1]
	v_cvt_pk_fp8_f32 v161, v86, v87 op_sel:[0,0,1]
	v_exp_f32_e32 v90, v90
	v_exp_f32_e32 v91, v91
	v_exp_f32_e32 v92, v92
	v_exp_f32_e32 v93, v93
	v_exp_f32_e32 v94, v94
	v_exp_f32_e32 v95, v95
	s_waitcnt lgkmcnt(0)
	v_mfma_scale_f32_32x32x64_f8f6f4 v[112:127], v[112:119], v[152:159], v[64:79], v173, v194 op_sel_hi:[0,0,0]
	s_setprio 0
	ds_read_b128 v[80:83], v224 offset:16384
	ds_read_b128 v[212:215], v224 offset:18432
	ds_read_b128 v[84:87], v225 offset:16384
	ds_read_b128 v[216:219], v225 offset:18432
	v_cvt_pk_fp8_f32 v162, v88, v89
	v_cvt_pk_fp8_f32 v163, v92, v93
	v_exp_f32_e32 v96, v96
	v_exp_f32_e32 v97, v97
	v_cvt_pk_fp8_f32 v162, v90, v91 op_sel:[0,0,1]
	v_cvt_pk_fp8_f32 v163, v94, v95 op_sel:[0,0,1]
	v_exp_f32_e32 v98, v98
	v_exp_f32_e32 v99, v99
	v_exp_f32_e32 v100, v100
	v_exp_f32_e32 v101, v101
	v_exp_f32_e32 v102, v102
	v_exp_f32_e32 v103, v103
	v_mfma_scale_f32_32x32x64_f8f6f4 v[128:143], v[128:135], v[152:159], v[64:79], v173, v194 op_sel_hi:[0,0,0]
	v_cvt_pk_fp8_f32 v164, v96, v97
	v_cvt_pk_fp8_f32 v165, v100, v101
	v_exp_f32_e32 v104, v104
	v_exp_f32_e32 v105, v105
	v_cvt_pk_fp8_f32 v164, v98, v99 op_sel:[0,0,1]
	v_cvt_pk_fp8_f32 v165, v102, v103 op_sel:[0,0,1]
	v_exp_f32_e32 v106, v106
	v_exp_f32_e32 v107, v107
	v_exp_f32_e32 v108, v108
	v_exp_f32_e32 v109, v109
	v_exp_f32_e32 v110, v110
	v_exp_f32_e32 v111, v111
	s_nop 0
	v_cvt_pk_fp8_f32 v166, v104, v105
	v_cvt_pk_fp8_f32 v167, v108, v109
	v_cvt_pk_fp8_f32 v166, v106, v107 op_sel:[0,0,1]
	v_cvt_pk_fp8_f32 v167, v110, v111 op_sel:[0,0,1]
	s_setprio 2
	s_waitcnt lgkmcnt(0)
	v_mfma_scale_f32_32x32x64_f8f6f4 v[32:47], v[80:87], v[160:167], v[32:47], v194, v194 op_sel_hi:[0,0,0]
	ds_read_b128 v[80:83], v222 offset:0
	ds_read_b128 v[96:99], v222 offset:2048
	ds_read_b128 v[84:87], v223 offset:0
	ds_read_b128 v[100:103], v223 offset:2048
	v_max3_f32 v227, v112, s5, v113
	v_max3_f32 v227, v227, v114, v115
	v_max3_f32 v227, v227, v116, v117
	v_max3_f32 v227, v227, v118, v119
	v_max3_f32 v227, v227, v120, v121
	v_max3_f32 v227, v227, v122, v123
	v_max3_f32 v227, v227, v124, v125
	v_max3_f32 v227, v227, v126, v127
	s_mov_b32 m0, s64
	s_add_u32 s42, s42, 0x2000
	s_addc_u32 s43, s43, 0
	global_load_lds_dwordx4 v221, s[44:45]
	v_mfma_scale_f32_32x32x64_f8f6f4 v[16:31], v[212:219], v[160:167], v[16:31], v194, v194 op_sel_hi:[0,0,0]
	v_max3_f32 v226, v128, s5, v129
	v_max3_f32 v226, v226, v130, v131
	v_max3_f32 v226, v226, v132, v133
	v_max3_f32 v226, v226, v134, v135
	v_max3_f32 v226, v226, v136, v137
	v_max3_f32 v226, v226, v138, v139
	v_max3_f32 v226, v226, v140, v141
	v_max3_f32 v226, v226, v142, v143
	s_mov_b32 m0, s65
	s_nop 0
	global_load_lds_dwordx4 v229, s[44:45]
	v_mfma_scale_f32_16x16x128_f8f6f4 v[48:51], v[144:151], v[160:167], v[48:51], v194, v194 op_sel_hi:[0,0,0]
	s_setprio 0
	v_max_f32_e32 v226, v227, v226
	v_cmp_lt_f32_e32 vcc, s36, v226
	s_cbranch_vccnz .Lat_rare_P15

	.amdhsa_kernel _Z13attn11_kernelILi4EEvPc
		.amdhsa_group_segment_fixed_size 16384
		.amdhsa_private_segment_fixed_size 0
		.amdhsa_kernarg_size 264
		.amdhsa_user_sgpr_count 2
		.amdhsa_user_sgpr_dispatch_ptr 0
		.amdhsa_user_sgpr_queue_ptr 0
		.amdhsa_user_sgpr_kernarg_segment_ptr 1
		.amdhsa_user_sgpr_dispatch_id 0
		.amdhsa_user_sgpr_kernarg_preload_length 0
		.amdhsa_user_sgpr_kernarg_preload_offset 0
		.amdhsa_user_sgpr_private_segment_size 0
		.amdhsa_uses_dynamic_stack 0
		.amdhsa_enable_private_segment 0
		.amdhsa_system_sgpr_workgroup_id_x 1
		.amdhsa_system_sgpr_workgroup_id_y 0
		.amdhsa_system_sgpr_workgroup_id_z 0
		.amdhsa_system_sgpr_workgroup_info 0
		.amdhsa_system_vgpr_workitem_id 0
		.amdhsa_next_free_vgpr 230
		.amdhsa_next_free_sgpr 68
		.amdhsa_accum_offset 232
		.amdhsa_reserve_vcc 1
		.amdhsa_float_round_mode_32 0
		.amdhsa_float_round_mode_16_64 0
		.amdhsa_float_denorm_mode_32 3
		.amdhsa_float_denorm_mode_16_64 3
		.amdhsa_dx10_clamp 1
		.amdhsa_ieee_mode 1
		.amdhsa_fp16_overflow 0
		.amdhsa_tg_split 0
		.amdhsa_exception_fp_ieee_invalid_op 0
		.amdhsa_exception_fp_denorm_src 0
		.amdhsa_exception_fp_ieee_div_zero 0
		.amdhsa_exception_fp_ieee_overflow 0
		.amdhsa_exception_fp_ieee_underflow 0
		.amdhsa_exception_fp_ieee_inexact 0
		.amdhsa_exception_int_div_zero 0
	.end_amdhsa_kernel

amdhsa.kernels:
  - .agpr_count:     0
    .args:
      - .actual_access:  read_only
        .address_space:  global
        .offset:         0
        .size:           8
        .value_kind:     global_buffer
      - .actual_access:  read_only
        .address_space:  global
        .offset:         8
        .size:           8
        .value_kind:     global_buffer
      - .actual_access:  read_only
        .address_space:  global
        .offset:         16
        .size:           8
        .value_kind:     global_buffer
      - .actual_access:  read_only
        .address_space:  global
        .offset:         24
        .size:           8
        .value_kind:     global_buffer
      - .actual_access:  read_only
        .address_space:  global
        .offset:         32
        .size:           8
        .value_kind:     global_buffer
      - .actual_access:  read_only
        .address_space:  global
        .offset:         40
        .size:           8
        .value_kind:     global_buffer
      - .actual_access:  read_only
        .address_space:  global
        .offset:         48
        .size:           8
        .value_kind:     global_buffer
      - .actual_access:  write_only
        .address_space:  global
        .offset:         56
        .size:           8
        .value_kind:     global_buffer
    .group_segment_fixed_size: 32
    .kernarg_segment_align: 8
    .kernarg_segment_size: 64
    .language:       OpenCL C
    .language_version:
      - 2
      - 0
    .max_flat_workgroup_size: 256
    .name:           _Z11prep_kernelPKfS0_S0_S0_S0_S0_S0_Pc
    .private_segment_fixed_size: 0
    .sgpr_count:     48
    .sgpr_spill_count: 0
    .symbol:         _Z11prep_kernelPKfS0_S0_S0_S0_S0_S0_Pc.kd
    .uniform_work_group_size: 1
    .uses_dynamic_stack: false
    .vgpr_count:     78
    .vgpr_spill_count: 0
    .wavefront_size: 64
  - .agpr_count:     0
    .args:
      - .address_space:  global
        .offset:         0
        .size:           8
        .value_kind:     global_buffer
      - .actual_access:  read_only
        .address_space:  global
        .offset:         8
        .size:           8
        .value_kind:     global_buffer
      - .actual_access:  read_only
        .address_space:  global
        .offset:         16
        .size:           8
        .value_kind:     global_buffer
    .group_segment_fixed_size: 0
    .kernarg_segment_align: 8
    .kernarg_segment_size: 24
    .language:       OpenCL C
    .language_version:
      - 2
      - 0
    .max_flat_workgroup_size: 512
    .name:           _Z13qkv256_kernelPcPKfS1_
    .private_segment_fixed_size: 0
    .sgpr_count:     35
    .sgpr_spill_count: 0
    .symbol:         _Z13qkv256_kernelPcPKfS1_.kd
    .uniform_work_group_size: 1
    .uses_dynamic_stack: false
    .vgpr_count:     214
    .vgpr_spill_count: 0
    .wavefront_size: 64
  - .agpr_count:     0
    .args:
      - .address_space:  global
        .offset:         0
        .size:           8
        .value_kind:     global_buffer
      - .actual_access:  read_only
        .address_space:  global
        .offset:         8
        .size:           8
        .value_kind:     global_buffer
      - .actual_access:  read_only
        .address_space:  global
        .offset:         16
        .size:           8
        .value_kind:     global_buffer
      - .actual_access:  write_only
        .address_space:  global
        .offset:         24
        .size:           8
        .value_kind:     global_buffer
    .group_segment_fixed_size: 0
    .kernarg_segment_align: 8
    .kernarg_segment_size: 32
    .language:       OpenCL C
    .language_version:
      - 2
      - 0
    .max_flat_workgroup_size: 256
    .name:           _Z11proj_kernelPKcPKfS2_Pf
    .private_segment_fixed_size: 0
    .sgpr_count:     34
    .sgpr_spill_count: 0
    .symbol:         _Z11proj_kernelPKcPKfS2_Pf.kd
    .uniform_work_group_size: 1
    .uses_dynamic_stack: false
    .vgpr_count:     185
    .vgpr_spill_count: 0
    .wavefront_size: 64
  - .agpr_count:     0
    .args:
      - .address_space:  global
        .offset:         0
        .size:           8
        .value_kind:     global_buffer
      - .offset:         8
        .size:           4
        .value_kind:     hidden_block_count_x
      - .offset:         12
        .size:           4
        .value_kind:     hidden_block_count_y
      - .offset:         16
        .size:           4
        .value_kind:     hidden_block_count_z
      - .offset:         20
        .size:           2
        .value_kind:     hidden_group_size_x
      - .offset:         22
        .size:           2
        .value_kind:     hidden_group_size_y
      - .offset:         24
        .size:           2
        .value_kind:     hidden_group_size_z
      - .offset:         26
        .size:           2
        .value_kind:     hidden_remainder_x
      - .offset:         28
        .size:           2
        .value_kind:     hidden_remainder_y
      - .offset:         30
        .size:           2
        .value_kind:     hidden_remainder_z
      - .offset:         48
        .size:           8
        .value_kind:     hidden_global_offset_x
      - .offset:         56
        .size:           8
        .value_kind:     hidden_global_offset_y
      - .offset:         64
        .size:           8
        .value_kind:     hidden_global_offset_z
      - .offset:         72
        .size:           2
        .value_kind:     hidden_grid_dims
      - .offset:         128
        .size:           4
        .value_kind:     hidden_dynamic_lds_size
    .group_segment_fixed_size: 16384
    .kernarg_segment_align: 8
    .kernarg_segment_size: 264
    .language:       OpenCL C
    .language_version:
      - 2
      - 0
    .max_flat_workgroup_size: 256
    .name:           _Z13attn11_kernelILi4EEvPc
    .private_segment_fixed_size: 0
    .sgpr_count:     74
    .sgpr_spill_count: 0
    .symbol:         _Z13attn11_kernelILi4EEvPc.kd
    .uniform_work_group_size: 1
    .uses_dynamic_stack: false
    .vgpr_count:     230
    .vgpr_spill_count: 0
    .wavefront_size: 64
